# baseline (speedup 1.0000x reference)
.LBB2_12:
	v_cmp_neq_f32_e32 vcc, s25, v102
	v_add_u32_e32 v114, v114, v98
	v_add_u32_e32 v107, 2, v107
	v_cndmask_b32_e64 v124, v112, -v102, vcc
	v_fmamk_f32 v34, v34, 0x3e38aa3b, v124
	v_fmamk_f32 v50, v50, 0x3e38aa3b, v124
	v_exp_f32_e32 v126, v34
	v_fmamk_f32 v34, v51, 0x3e38aa3b, v124
	v_exp_f32_e32 v125, v50
	v_exp_f32_e32 v82, v34
	v_fmamk_f32 v34, v35, 0x3e38aa3b, v124
	v_exp_f32_e32 v34, v34
	v_add_f32_e32 v35, v126, v125
	v_fmamk_f32 v36, v36, 0x3e38aa3b, v124
	v_exp_f32_e32 v127, v36
	v_pk_add_f32 v[50:51], v[34:35], v[82:83]
	v_fmamk_f32 v35, v52, 0x3e38aa3b, v124
	v_pk_add_f32 v[88:89], v[50:51], v[50:51] op_sel_hi:[0,1]
	v_fmamk_f32 v36, v53, 0x3e38aa3b, v124
	v_exp_f32_e32 v35, v35
	v_exp_f32_e32 v88, v36
	v_fmamk_f32 v36, v37, 0x3e38aa3b, v124
	v_exp_f32_e32 v36, v36
	v_add_f32_e32 v37, v127, v35
	v_fmamk_f32 v38, v38, 0x3e38aa3b, v124
	v_exp_f32_e32 v115, v38
	v_pk_add_f32 v[50:51], v[36:37], v[88:89]
	v_fmamk_f32 v37, v54, 0x3e38aa3b, v124
	v_pk_add_f32 v[90:91], v[50:51], v[50:51] op_sel_hi:[0,1]
	v_fmamk_f32 v38, v55, 0x3e38aa3b, v124
	v_exp_f32_e32 v37, v37
	v_exp_f32_e32 v90, v38
	v_fmamk_f32 v38, v39, 0x3e38aa3b, v124
	v_exp_f32_e32 v50, v38
	v_add_f32_e32 v51, v115, v37
	v_pk_add_f32 v[38:39], v[50:51], v[90:91]
	v_pk_add_f32 v[54:55], v[38:39], v[38:39] op_sel_hi:[0,1]
	v_fmamk_f32 v38, v56, 0x3e38aa3b, v124
	v_exp_f32_e32 v51, v38
	v_fmamk_f32 v38, v40, 0x3e38aa3b, v124
	v_exp_f32_e32 v91, v38
	v_fmamk_f32 v38, v57, 0x3e38aa3b, v124
	v_exp_f32_e32 v54, v38
	v_fmamk_f32 v38, v41, 0x3e38aa3b, v124
	v_exp_f32_e32 v52, v38
	s_nop 0
	s_add_i32 s16, s22, 0xffffc000
	s_and_b32 s16, s16, 0xc000
	v_add_u32_e32 v122, s16, v108
	s_add_u32 s16, s12, 0xfffce000
	s_addc_u32 s17, s13, -1
	v_readfirstlane_b32 s26, v122
	v_lshl_add_u64 v[122:123], s[16:17], 0, v[84:85]
	s_mov_b32 s27, m0
	s_mov_b32 m0, s26
	s_nop 0
	global_load_lds_dwordx4 v[122:123], off
	s_mov_b32 m0, s27
	v_lshl_add_u64 v[122:123], s[16:17], 0, v[86:87]
	s_add_i32 s16, s26, 0x400
	s_mov_b32 s17, m0
	s_mov_b32 m0, s16
	s_nop 0
	global_load_lds_dwordx4 v[122:123], off
	s_mov_b32 m0, s17
	s_and_b32 s16, s22, 0xc000
	v_add_u32_e32 v122, s16, v108
	s_nop 0
	v_readfirstlane_b32 s16, v122
	v_lshl_add_u64 v[122:123], s[12:13], 0, v[84:85]
	s_mov_b32 s17, m0
	s_mov_b32 m0, s16
	s_nop 0
	global_load_lds_dwordx4 v[122:123], off
	s_mov_b32 m0, s17
	v_lshl_add_u64 v[122:123], s[12:13], 0, v[86:87]
	s_addk_i32 s16, 0x400
	s_mov_b32 s17, m0
	s_mov_b32 m0, s16
	s_nop 0
	global_load_lds_dwordx4 v[122:123], off
	s_mov_b32 m0, s17
	s_add_u32 s12, s12, 0x64000
	s_addc_u32 s13, s13, 0
	s_add_i32 s22, s22, 0x8000
	v_add_f32_e32 v53, v91, v51
	v_cvt_pk_f16_f32 v57, v51, v54
	v_cvt_pk_f16_f32 v56, v37, v90
	v_pk_add_f32 v[38:39], v[52:53], v[54:55]
	v_cvt_pk_f16_f32 v55, v35, v88
	v_pk_add_f32 v[116:117], v[38:39], v[38:39] op_sel_hi:[0,1]
	v_fmamk_f32 v38, v58, 0x3e38aa3b, v124
	v_exp_f32_e32 v53, v38
	v_fmamk_f32 v38, v42, 0x3e38aa3b, v124
	v_exp_f32_e32 v1, v38
	v_fmamk_f32 v38, v59, 0x3e38aa3b, v124
	v_exp_f32_e32 v116, v38
	v_fmamk_f32 v38, v43, 0x3e38aa3b, v124
	v_exp_f32_e32 v38, v38
	v_add_f32_e32 v39, v1, v53
	v_cvt_pk_f16_f32 v54, v125, v82
	v_fmamk_f32 v35, v64, 0x3e38aa3b, v124
	v_pk_add_f32 v[40:41], v[38:39], v[116:117]
	v_fmamk_f32 v39, v60, 0x3e38aa3b, v124
	v_pk_add_f32 v[118:119], v[40:41], v[40:41] op_sel_hi:[0,1]
	v_fmamk_f32 v40, v44, 0x3e38aa3b, v124
	v_exp_f32_e32 v117, v40
	v_fmamk_f32 v40, v61, 0x3e38aa3b, v124
	v_exp_f32_e32 v39, v39
	v_exp_f32_e32 v118, v40
	v_fmamk_f32 v40, v45, 0x3e38aa3b, v124
	v_exp_f32_e32 v40, v40
	v_add_f32_e32 v41, v117, v39
	v_exp_f32_e32 v82, v35
	v_fmamk_f32 v35, v65, 0x3e38aa3b, v124
	v_pk_add_f32 v[42:43], v[40:41], v[118:119]
	v_fmamk_f32 v41, v62, 0x3e38aa3b, v124
	v_pk_add_f32 v[120:121], v[42:43], v[42:43] op_sel_hi:[0,1]
	v_fmamk_f32 v42, v46, 0x3e38aa3b, v124
	v_exp_f32_e32 v119, v42
	v_fmamk_f32 v42, v63, 0x3e38aa3b, v124
	v_exp_f32_e32 v41, v41
	v_exp_f32_e32 v120, v42
	v_fmamk_f32 v42, v47, 0x3e38aa3b, v124
	v_exp_f32_e32 v122, v42
	ds_read_b64_tr_b16 v[42:43], v114 offset:8192
	ds_read_b64_tr_b16 v[44:45], v114 offset:8704
	v_add_f32_e32 v123, v119, v41
	ds_read_b64_tr_b16 v[58:59], v114 offset:9216
	ds_read_b64_tr_b16 v[60:61], v114 offset:9728
	v_pk_add_f32 v[46:47], v[122:123], v[120:121]
	s_waitcnt lgkmcnt(2)
	v_mfma_f32_32x32x16_f16 v[18:33], v[54:57], v[42:45], v[18:33]
	v_add_f32_e64 v88, v46, v46
	v_add_f32_e64 v89, v46, v47
	ds_read_b64_tr_b16 v[42:43], v114 offset:12288
	ds_read_b64_tr_b16 v[44:45], v114 offset:12800
	v_exp_f32_e32 v88, v35
	ds_read_b64_tr_b16 v[62:63], v114 offset:13312
	ds_read_b64_tr_b16 v[64:65], v114 offset:13824
	v_cvt_pk_f16_f32 v51, v127, v36
	v_cmp_le_u32_e32 vcc, s21, v107
	s_or_b64 s[14:15], vcc, s[14:15]
	s_waitcnt lgkmcnt(2)
	v_mfma_f32_32x32x16_f16 v[2:17], v[54:57], v[42:45], v[2:17]
	v_cvt_pk_f16_f32 v45, v82, v88
	v_cvt_pk_f16_f32 v44, v41, v120
	v_cvt_pk_f16_f32 v43, v39, v118
	v_cvt_pk_f16_f32 v42, v53, v116
	v_cvt_pk_f16_f32 v53, v91, v52
	v_cvt_pk_f16_f32 v52, v115, v50
	v_cvt_pk_f16_f32 v50, v126, v34
	v_mfma_f32_32x32x16_f16 v[18:33], v[42:45], v[58:61], v[18:33]
	v_fmamk_f32 v39, v48, 0x3e38aa3b, v124
	v_fmac_f32_e32 v124, 0x3e38aa3b, v49
	v_exp_f32_e32 v39, v39
	v_exp_f32_e32 v54, v124
	v_cvt_pk_f16_f32 v41, v117, v40
	v_cvt_pk_f16_f32 v40, v1, v38
	v_add_f32_e32 v55, v39, v82
	s_waitcnt lgkmcnt(0)
	v_mfma_f32_32x32x16_f16 v[2:17], v[42:45], v[62:65], v[2:17]
	ds_read_b64_tr_b16 v[42:43], v114 offset:10240
	ds_read_b64_tr_b16 v[44:45], v114 offset:10752
	ds_read_b64_tr_b16 v[34:35], v114 offset:11264
	ds_read_b64_tr_b16 v[36:37], v114 offset:11776
	s_waitcnt lgkmcnt(2)
	v_mfma_f32_32x32x16_f16 v[18:33], v[50:53], v[42:45], v[18:33]
	ds_read_b64_tr_b16 v[42:43], v114 offset:14336
	ds_read_b64_tr_b16 v[44:45], v114 offset:14848
	ds_read_b64_tr_b16 v[46:47], v114 offset:15360
	ds_read_b64_tr_b16 v[48:49], v114 offset:15872
	s_waitcnt lgkmcnt(2)
	v_mfma_f32_32x32x16_f16 v[2:17], v[50:53], v[42:45], v[2:17]
	v_cvt_pk_f16_f32 v43, v39, v54
	v_cvt_pk_f16_f32 v42, v119, v122
	s_nop 1
	v_mfma_f32_32x32x16_f16 v[18:33], v[40:43], v[34:37], v[18:33]
	v_add_f32_e64 v34, v54, v88
	v_add_f32_e64 v35, v55, v89
	v_mov_b32_e32 v88, v102
	v_add_f32_e32 v1, v34, v35
	v_add_f32_e32 v113, v113, v1
	s_waitcnt lgkmcnt(0)
	v_mfma_f32_32x32x16_f16 v[2:17], v[40:43], v[46:49], v[2:17]
	s_andn2_b64 exec, exec, s[14:15]
	s_cbranch_execz .LBB2_17
